# baseline (speedup 1.0000x reference)
_Z11prep_kernelPKfS0_S0_S0_S0_S0_S0_PDF16_S1_:
	s_cmpk_gt_i32 s2, 0x47f
	s_cbranch_scc0 .LBB0_2
	s_add_i32 s12, s2, 0xfffffb80
	s_load_dwordx2 s[8:9], s[0:1], 0x40
	s_load_dwordx4 s[4:7], s[0:1], 0x20
	s_load_dwordx2 s[10:11], s[0:1], 0x30
	s_mul_hi_u32 s3, s12, 0xaaaaaaab
	s_lshr_b32 s13, s3, 10
	s_mul_i32 s3, s13, 0xfffffa00
	s_add_i32 s3, s3, s12
	s_and_b32 s15, s3, 7
	s_lshr_b32 s3, s3, 3
	s_cmp_ge_u32 s3, 96
	s_cselect_b32 s16, 8, 0
	s_cselect_b32 s17, 96, 0
	s_sub_i32 s3, s3, s17
	s_add_i32 s16, s16, s15
	s_mul_i32 s16, s16, 96
	s_add_i32 s3, s16, s3
	s_add_i32 s14, s2, 0xfffff580
	s_cmpk_lt_u32 s14, 0x600
	s_waitcnt lgkmcnt(0)
	s_cselect_b32 s6, s6, s10
	s_cselect_b32 s7, s7, s11
	s_cmpk_lt_u32 s12, 0x600
	s_cselect_b32 s5, s5, s7
	s_mul_hi_u32 s7, s13, 0x600000
	s_mul_i32 s13, s13, 0x600000
	s_cselect_b32 s4, s4, s6
	s_add_u32 s6, s8, s13
	s_addc_u32 s7, s9, s7
	s_cbranch_execz .LBB0_3
	s_branch .LBB0_7

	.amdhsa_kernel _Z11prep_kernelPKfS0_S0_S0_S0_S0_S0_PDF16_S1_
		.amdhsa_group_segment_fixed_size 0
		.amdhsa_private_segment_fixed_size 0
		.amdhsa_kernarg_size 72
		.amdhsa_user_sgpr_count 2
		.amdhsa_user_sgpr_dispatch_ptr 0
		.amdhsa_user_sgpr_queue_ptr 0
		.amdhsa_user_sgpr_kernarg_segment_ptr 1
		.amdhsa_user_sgpr_dispatch_id 0
		.amdhsa_user_sgpr_kernarg_preload_length 0
		.amdhsa_user_sgpr_kernarg_preload_offset 0
		.amdhsa_user_sgpr_private_segment_size 0
		.amdhsa_uses_dynamic_stack 0
		.amdhsa_enable_private_segment 0
		.amdhsa_system_sgpr_workgroup_id_x 1
		.amdhsa_system_sgpr_workgroup_id_y 0
		.amdhsa_system_sgpr_workgroup_id_z 0
		.amdhsa_system_sgpr_workgroup_info 0
		.amdhsa_system_vgpr_workitem_id 0
		.amdhsa_next_free_vgpr 10
		.amdhsa_next_free_sgpr 20
		.amdhsa_accum_offset 12
		.amdhsa_reserve_vcc 1
		.amdhsa_float_round_mode_32 0
		.amdhsa_float_round_mode_16_64 0
		.amdhsa_float_denorm_mode_32 3
		.amdhsa_float_denorm_mode_16_64 3
		.amdhsa_dx10_clamp 1
		.amdhsa_ieee_mode 1
		.amdhsa_fp16_overflow 0
		.amdhsa_tg_split 0
		.amdhsa_exception_fp_ieee_invalid_op 0
		.amdhsa_exception_fp_denorm_src 0
		.amdhsa_exception_fp_ieee_div_zero 0
		.amdhsa_exception_fp_ieee_overflow 0
		.amdhsa_exception_fp_ieee_underflow 0
		.amdhsa_exception_fp_ieee_inexact 0
		.amdhsa_exception_int_div_zero 0
	.end_amdhsa_kernel

_Z14combine_kernelPKDF16_PK15HIP_vector_typeIfLj2EEPDF16_:
	s_load_dwordx4 s[4:7], s[0:1], 0x0
	s_load_dwordx2 s[8:9], s[0:1], 0x10
	s_and_b32 s10, s2, 7
	s_lshr_b32 s11, s2, 3
	s_mul_hi_u32 s12, s11, 0xaaaaaab
	s_mul_i32 s13, s12, 24
	s_sub_i32 s11, s11, s13
	s_lshl_b32 s12, s12, 3
	s_or_b32 s12, s12, s10
	s_mul_i32 s12, s12, 24
	s_add_i32 s2, s12, s11
	v_lshl_or_b32 v0, s2, 8, v0
	s_mov_b32 s0, 0x2aaaaaab
	v_mul_hi_i32 v1, v0, s0
	v_lshrrev_b32_e32 v2, 31, v1
	v_ashrrev_i32_e32 v1, 3, v1
	v_add_u32_e32 v10, v1, v2
	s_movk_i32 s0, 0xffd0
	v_mad_u64_u32 v[2:3], s[0:1], v10, s0, v[0:1]
	v_ashrrev_i32_e32 v1, 31, v0
	v_lshlrev_b64 v[16:17], 5, v[0:1]
	v_ashrrev_i32_e32 v11, 2, v2
	v_ashrrev_i32_e32 v12, 11, v10
	s_waitcnt lgkmcnt(0)
	v_lshl_add_u64 v[8:9], s[4:5], 0, v[16:17]
	s_mov_b64 s[0:1], 0x600000
	v_and_b32_e32 v24, 0x7ff, v10
	v_mad_i32_i24 v10, v12, 12, v11
	v_lshl_add_u64 v[20:21], v[8:9], 0, s[0:1]
	s_mov_b32 s0, 0x600000
	v_ashrrev_i32_e32 v11, 31, v10
	v_add_co_u32_e32 v22, vcc, s0, v8
	v_lshlrev_b64 v[18:19], 14, v[10:11]
	s_nop 0
	v_addc_co_u32_e32 v23, vcc, 0, v9, vcc
	global_load_dwordx4 v[0:3], v[8:9], off nt
	global_load_dwordx4 v[4:7], v[8:9], off offset:16 nt
	s_nop 0
	global_load_dwordx4 v[8:11], v[22:23], off nt
	global_load_dwordx4 v[12:15], v[20:21], off offset:16 nt
	v_lshl_add_u64 v[18:19], s[6:7], 0, v[18:19]
	v_lshlrev_b32_e32 v20, 3, v24
	v_mov_b32_e32 v21, 0
	v_lshl_add_u64 v[18:19], v[18:19], 0, v[20:21]
	s_mov_b32 s0, 0x60000
	v_add_co_u32_e32 v20, vcc, s0, v18
	s_waitcnt vmcnt(3)
	v_cvt_f32_f16_e32 v41, v3
	v_addc_co_u32_e32 v21, vcc, 0, v19, vcc
	global_load_dwordx2 v[22:23], v[18:19], off
	global_load_dwordx2 v[24:25], v[20:21], off
	s_waitcnt vmcnt(4)
	v_cvt_f32_f16_sdwa v37, v6 dst_sel:DWORD dst_unused:UNUSED_PAD src0_sel:WORD_1
	v_cvt_f32_f16_e32 v38, v6
	v_cvt_f32_f16_sdwa v43, v3 dst_sel:DWORD dst_unused:UNUSED_PAD src0_sel:WORD_1
	v_cvt_f32_f16_e32 v21, v1
	v_cvt_f32_f16_sdwa v34, v1 dst_sel:DWORD dst_unused:UNUSED_PAD src0_sel:WORD_1
	s_waitcnt vmcnt(3)
	v_cvt_f32_f16_e32 v1, v8
	v_cvt_f32_f16_sdwa v20, v8 dst_sel:DWORD dst_unused:UNUSED_PAD src0_sel:WORD_1
	v_cvt_f32_f16_e32 v27, v9
	v_cvt_f32_f16_sdwa v32, v9 dst_sel:DWORD dst_unused:UNUSED_PAD src0_sel:WORD_1
	v_cvt_f32_f16_e32 v35, v10
	v_cvt_f32_f16_sdwa v40, v10 dst_sel:DWORD dst_unused:UNUSED_PAD src0_sel:WORD_1
	v_cvt_f32_f16_sdwa v29, v5 dst_sel:DWORD dst_unused:UNUSED_PAD src0_sel:WORD_1
	v_cvt_f32_f16_e32 v30, v5
	s_waitcnt vmcnt(2)
	v_cvt_f32_f16_e32 v18, v12
	v_cvt_f32_f16_sdwa v5, v12 dst_sel:DWORD dst_unused:UNUSED_PAD src0_sel:WORD_1
	v_cvt_f32_f16_e32 v28, v13
	v_cvt_f32_f16_sdwa v31, v13 dst_sel:DWORD dst_unused:UNUSED_PAD src0_sel:WORD_1
	v_cvt_f32_f16_sdwa v42, v11 dst_sel:DWORD dst_unused:UNUSED_PAD src0_sel:WORD_1
	v_cvt_f32_f16_e32 v36, v14
	v_cvt_f32_f16_sdwa v39, v14 dst_sel:DWORD dst_unused:UNUSED_PAD src0_sel:WORD_1
	v_cvt_f32_f16_sdwa v19, v4 dst_sel:DWORD dst_unused:UNUSED_PAD src0_sel:WORD_1
	v_cvt_f32_f16_e32 v4, v4
	v_cvt_f32_f16_sdwa v26, v0 dst_sel:DWORD dst_unused:UNUSED_PAD src0_sel:WORD_1
	v_cvt_f32_f16_e32 v33, v2
	v_cvt_f32_f16_sdwa v2, v2 dst_sel:DWORD dst_unused:UNUSED_PAD src0_sel:WORD_1
	s_waitcnt vmcnt(1)
	v_max_f32_e32 v3, v22, v22
	s_waitcnt vmcnt(0)
	v_max_f32_e32 v6, v24, v24
	v_max_f32_e32 v3, v3, v6
	v_sub_f32_e32 v6, v22, v3
	v_sub_f32_e32 v3, v24, v3
	v_exp_f32_e32 v9, v6
	v_exp_f32_e32 v8, v3
	v_mov_b32_e32 v22, v25
	v_cvt_f32_f16_e32 v3, v11
	v_pk_mul_f32 v[8:9], v[22:23], v[8:9]
	s_nop 0
	v_add_f32_e32 v6, v9, v8
	v_div_scale_f32 v10, s[0:1], v6, v6, 1.0
	v_rcp_f32_e32 v12, v10
	v_div_scale_f32 v11, vcc, 1.0, v6, 1.0
	v_fma_f32 v13, -v10, v12, 1.0
	v_fmac_f32_e32 v12, v13, v12
	v_mul_f32_e32 v13, v11, v12
	v_fma_f32 v14, -v10, v13, v11
	v_fmac_f32_e32 v13, v14, v12
	v_fma_f32 v10, -v10, v13, v11
	v_div_fmas_f32 v10, v10, v12, v13
	v_div_fixup_f32 v6, v10, v6, 1.0
	v_pk_mul_f32 v[8:9], v[8:9], v[6:7] op_sel_hi:[1,0]
	s_nop 0
	v_mul_f32_e32 v1, v8, v1
	v_pk_mul_f32 v[4:5], v[8:9], v[4:5] op_sel:[1,0] op_sel_hi:[0,1]
	v_pk_mul_f32 v[10:11], v[8:9], v[26:27] op_sel:[1,0] op_sel_hi:[0,1]
	v_pk_mul_f32 v[12:13], v[8:9], v[30:31] op_sel:[1,0] op_sel_hi:[0,1]
	v_pk_mul_f32 v[22:23], v[8:9], v[34:35] op_sel:[1,0] op_sel_hi:[0,1]
	v_pk_mul_f32 v[2:3], v[8:9], v[2:3] op_sel:[1,0] op_sel_hi:[0,1]
	v_fma_mixlo_f16 v6, v9, v0, v1 op_sel_hi:[0,1,0]
	v_pk_fma_f32 v[0:1], v[8:9], v[18:19], v[4:5]
	v_pk_fma_f32 v[4:5], v[8:9], v[20:21], v[10:11]
	v_pk_fma_f32 v[10:11], v[8:9], v[28:29], v[12:13]
	v_pk_fma_f32 v[12:13], v[8:9], v[32:33], v[22:23]
	v_pk_fma_f32 v[20:21], v[8:9], v[40:41], v[2:3]
	v_cvt_pk_f16_f32 v0, v0, v1
	v_cvt_pk_f16_f32 v3, v4, v5
	v_cvt_pk_f16_f32 v1, v10, v11
	v_cvt_pk_f16_f32 v14, v12, v13
	v_pk_mul_f32 v[10:11], v[8:9], v[42:43]
	v_cvt_f32_f16_e32 v12, v7
	v_cvt_f32_f16_sdwa v13, v15 dst_sel:DWORD dst_unused:UNUSED_PAD src0_sel:WORD_1
	v_pack_b32_f16 v4, v6, v3
	v_alignbit_b32 v5, v14, v3, 16
	v_add_f32_e32 v3, v11, v10
	v_cvt_f32_f16_sdwa v11, v7 dst_sel:DWORD dst_unused:UNUSED_PAD src0_sel:WORD_1
	v_cvt_f32_f16_e32 v10, v15
	v_cvt_f16_f32_e32 v3, v3
	v_pk_mul_f32 v[24:25], v[8:9], v[38:39] op_sel:[1,0] op_sel_hi:[0,1]
	v_pk_fma_f32 v[18:19], v[8:9], v[36:37], v[24:25]
	v_pk_mul_f32 v[12:13], v[8:9], v[12:13] op_sel:[1,0] op_sel_hi:[0,1]
	v_cvt_pk_f16_f32 v2, v18, v19
	v_cvt_pk_f16_f32 v18, v20, v21
	v_pk_fma_f32 v[8:9], v[8:9], v[10:11], v[12:13]
	v_alignbit_b32 v6, v18, v14, 16
	v_alignbit_b32 v7, v3, v18, 16
	v_cvt_pk_f16_f32 v3, v8, v9
	v_lshl_add_u64 v[8:9], s[8:9], 0, v[16:17]
	global_store_dwordx4 v[8:9], v[4:7], off
	global_store_dwordx4 v[8:9], v[0:3], off offset:16
	s_endpgm

	.amdhsa_kernel _Z14combine_kernelPKDF16_PK15HIP_vector_typeIfLj2EEPDF16_
		.amdhsa_group_segment_fixed_size 0
		.amdhsa_private_segment_fixed_size 0
		.amdhsa_kernarg_size 24
		.amdhsa_user_sgpr_count 2
		.amdhsa_user_sgpr_dispatch_ptr 0
		.amdhsa_user_sgpr_queue_ptr 0
		.amdhsa_user_sgpr_kernarg_segment_ptr 1
		.amdhsa_user_sgpr_dispatch_id 0
		.amdhsa_user_sgpr_kernarg_preload_length 0
		.amdhsa_user_sgpr_kernarg_preload_offset 0
		.amdhsa_user_sgpr_private_segment_size 0
		.amdhsa_uses_dynamic_stack 0
		.amdhsa_enable_private_segment 0
		.amdhsa_system_sgpr_workgroup_id_x 1
		.amdhsa_system_sgpr_workgroup_id_y 0
		.amdhsa_system_sgpr_workgroup_id_z 0
		.amdhsa_system_sgpr_workgroup_info 0
		.amdhsa_system_vgpr_workitem_id 0
		.amdhsa_next_free_vgpr 44
		.amdhsa_next_free_sgpr 16
		.amdhsa_accum_offset 44
		.amdhsa_reserve_vcc 1
		.amdhsa_float_round_mode_32 0
		.amdhsa_float_round_mode_16_64 0
		.amdhsa_float_denorm_mode_32 3
		.amdhsa_float_denorm_mode_16_64 3
		.amdhsa_dx10_clamp 1
		.amdhsa_ieee_mode 1
		.amdhsa_fp16_overflow 0
		.amdhsa_tg_split 0
		.amdhsa_exception_fp_ieee_invalid_op 0
		.amdhsa_exception_fp_denorm_src 0
		.amdhsa_exception_fp_ieee_div_zero 0
		.amdhsa_exception_fp_ieee_overflow 0
		.amdhsa_exception_fp_ieee_underflow 0
		.amdhsa_exception_fp_ieee_inexact 0
		.amdhsa_exception_int_div_zero 0
	.end_amdhsa_kernel
